# v63 + final rmsnorm phase: non-temporal hint on the once-read h rows and on the never-re-read f32 output stores
# speedup vs baseline: 1.0077x; 1.0031x over previous
; __device__ __forceinline__ float bf2f(unsigned v) { return __uint_as_float(v << 16); }
; __device__ __forceinline__ void phase_final(Frame& F) {
;     ...
;     for (int row0 = 4 * F.gw(); row0 < T; row0 += 4 * F.ngw()) {
;         u32x2 w[4][4];
; #pragma unroll
;         for (int q = 0; q < 4; ++q) { const u32x2* xr = (const u32x2*)(H + (size_t)(row0 + q) * DM) + F.lane;
; #pragma unroll
;             for (int j = 0; j < 4; ++j) w[q][j] = xr[64 * j]; }
; #pragma unroll
;         for (int q = 0; q < 4; ++q) { f32x4 v[4]; float s = 0.f;
; #pragma unroll
;             for (int j = 0; j < 4; ++j) { v[j] = (f32x4){bf2f(w[q][j].x & 0xffffu), bf2f(w[q][j].x >> 16), bf2f(w[q][j].y & 0xffffu), bf2f(w[q][j].y >> 16)}; s += (v[j][0] * v[j][0] + v[j][1] * v[j][1]) + (v[j][2] * v[j][2] + v[j][3] * v[j][3]); }
.LBB0_1563:
	v_add_co_u32_e32 v24, vcc, 0xffffe200, v18
	v_add_co_u32_e64 v20, s[0:1], s16, v16
	s_nop 0
	v_addc_co_u32_e32 v25, vcc, -1, v19, vcc
	v_add_co_u32_e32 v28, vcc, 0xffffe400, v18
	v_addc_co_u32_e64 v21, s[0:1], -1, v17, s[0:1]
	s_nop 0
	v_addc_co_u32_e32 v29, vcc, -1, v19, vcc
	v_add_co_u32_e32 v30, vcc, 0xffffe600, v18
	flat_load_dwordx2 v[32:33], v[24:25] nt
	flat_load_dwordx2 v[34:35], v[28:29] nt
	v_addc_co_u32_e32 v31, vcc, -1, v19, vcc
	v_add_co_u32_e32 v24, vcc, 0xffffe800, v18
	v_add_co_u32_e64 v22, s[0:1], s17, v16
	s_nop 0
	v_addc_co_u32_e32 v25, vcc, -1, v19, vcc
	v_add_co_u32_e32 v28, vcc, 0xffffea00, v18
	flat_load_dwordx2 v[36:37], v[30:31] nt
	flat_load_dwordx2 v[42:43], v[24:25] nt
	v_addc_co_u32_e32 v29, vcc, -1, v19, vcc
	v_add_co_u32_e32 v24, vcc, 0xffffec00, v18
	v_addc_co_u32_e64 v23, s[0:1], -1, v17, s[0:1]
	s_nop 0
	v_addc_co_u32_e32 v25, vcc, -1, v19, vcc
	v_add_co_u32_e32 v30, vcc, 0xffffee00, v18
	flat_load_dwordx2 v[48:49], v[28:29] nt
	flat_load_dwordx2 v[50:51], v[24:25] nt
	v_addc_co_u32_e32 v31, vcc, -1, v19, vcc
	v_add_co_u32_e32 v24, vcc, 0xfffff000, v18
	v_add_co_u32_e64 v26, s[0:1], s9, v16
	s_nop 0
	v_addc_co_u32_e32 v25, vcc, -1, v19, vcc
	v_add_co_u32_e32 v28, vcc, 0xfffff200, v18
	flat_load_dwordx2 v[52:53], v[30:31] nt
	flat_load_dwordx2 v[54:55], v[24:25] nt
	v_addc_co_u32_e32 v29, vcc, -1, v19, vcc
	v_add_co_u32_e32 v24, vcc, 0xfffff400, v18
	v_addc_co_u32_e64 v27, s[0:1], -1, v17, s[0:1]
	s_nop 0
	v_addc_co_u32_e32 v25, vcc, -1, v19, vcc
	v_add_co_u32_e32 v30, vcc, 0xfffff600, v18
	flat_load_dwordx2 v[62:63], v[28:29] nt
	flat_load_dwordx2 v[64:65], v[24:25] nt
	v_addc_co_u32_e32 v31, vcc, -1, v19, vcc
	v_add_co_u32_e32 v24, vcc, 0xfffff800, v18
	s_add_i32 s8, s8, s10
	s_nop 0
	v_addc_co_u32_e32 v25, vcc, -1, v19, vcc
	v_add_co_u32_e32 v28, vcc, 0xfffffa00, v18
	flat_load_dwordx2 v[66:67], v[30:31] nt
	flat_load_dwordx2 v[70:71], v[24:25] nt
	v_addc_co_u32_e32 v29, vcc, -1, v19, vcc
	v_add_co_u32_e32 v24, vcc, 0xfffffc00, v18
	flat_load_dwordx2 v[76:77], v[28:29] nt
	s_nop 0
	v_addc_co_u32_e32 v25, vcc, -1, v19, vcc
	v_add_co_u32_e32 v28, vcc, 0xfffffe00, v18
	s_cmp_lt_i32 s8, 0x8000
	s_nop 0
	v_addc_co_u32_e32 v29, vcc, -1, v19, vcc
	flat_load_dwordx2 v[78:79], v[24:25] nt
	flat_load_dwordx2 v[82:83], v[28:29] nt
	flat_load_dwordx2 v[84:85], v[18:19] nt
	v_lshl_add_u64 v[18:19], v[18:19], 0, s[14:15]
	s_waitcnt vmcnt(0) lgkmcnt(0)
	v_and_b32_e32 v25, 0xffff0000, v32
	v_and_b32_e32 v29, 0xffff0000, v33
	v_lshlrev_b32_e32 v24, 16, v32
	v_lshlrev_b32_e32 v28, 16, v33
	v_mul_f32_e32 v32, v29, v29
	v_and_b32_e32 v31, 0xffff0000, v35
	v_and_b32_e32 v30, 0xffff0000, v34
	v_mul_f32_e32 v40, v25, v25
	v_lshlrev_b32_e32 v45, 16, v35
	v_lshlrev_b32_e32 v44, 16, v34
	v_pk_fma_f32 v[32:33], v[28:29], v[28:29], v[32:33] op_sel_hi:[1,1,0]
	v_pk_mul_f32 v[46:47], v[30:31], v[30:31]
	v_lshlrev_b32_e32 v34, 16, v36
	v_and_b32_e32 v35, 0xffff0000, v36
	v_lshlrev_b32_e32 v38, 16, v37
	v_and_b32_e32 v39, 0xffff0000, v37
	v_pk_fma_f32 v[36:37], v[24:25], v[24:25], v[40:41] op_sel_hi:[1,1,0]
	v_lshlrev_b32_e32 v59, 16, v42
	v_mov_b32_e32 v40, v44
	v_mov_b32_e32 v41, v30
	v_mov_b32_e32 v30, v45
	v_pk_fma_f32 v[56:57], v[44:45], v[44:45], v[46:47]
	v_and_b32_e32 v47, 0xffff0000, v42
	v_lshlrev_b32_e32 v44, 16, v43
	v_and_b32_e32 v45, 0xffff0000, v43
	v_mov_b32_e32 v58, v36
	v_mov_b32_e32 v42, v32
	v_pk_add_f32 v[60:61], v[36:37], v[32:33]
	v_mul_f32_e32 v32, v35, v35
	v_mul_f32_e32 v36, v39, v39
	v_mov_b32_e32 v43, v59
	v_mul_f32_e32 v61, v47, v47
	v_mul_f32_e32 v74, v44, v44
	v_mul_f32_e32 v75, v45, v45
	v_pk_add_f32 v[68:69], v[56:57], v[56:57] op_sel:[0,1] op_sel_hi:[1,0]
	v_pk_fma_f32 v[56:57], v[34:35], v[34:35], v[32:33] op_sel_hi:[1,1,0]
	v_pk_fma_f32 v[72:73], v[38:39], v[38:39], v[36:37] op_sel_hi:[1,1,0]
	v_lshlrev_b32_e32 v32, 16, v48
	v_and_b32_e32 v33, 0xffff0000, v48
	v_lshlrev_b32_e32 v36, 16, v49
	v_and_b32_e32 v37, 0xffff0000, v49
	v_pk_mul_f32 v[48:49], v[58:59], v[42:43]
	v_and_b32_e32 v43, 0xffff0000, v51
	v_and_b32_e32 v42, 0xffff0000, v50
	v_mov_b32_e32 v46, v59
	v_mov_b32_e32 v69, v61
	v_mov_b32_e32 v57, v74
	v_mov_b32_e32 v73, v75
	v_mul_f32_e32 v48, v37, v37
	v_lshlrev_b32_e32 v59, 16, v51
	v_lshlrev_b32_e32 v58, 16, v50
	v_mul_f32_e32 v74, v33, v33
	v_mov_b32_e32 v61, v49
	v_pk_mul_f32 v[86:87], v[42:43], v[42:43]
	v_pk_add_f32 v[72:73], v[56:57], v[72:73]
	v_pk_fma_f32 v[80:81], v[36:37], v[36:37], v[48:49] op_sel_hi:[1,1,0]
	v_lshlrev_b32_e32 v48, 16, v52
	v_and_b32_e32 v49, 0xffff0000, v52
	v_lshlrev_b32_e32 v50, 16, v53
	v_and_b32_e32 v51, 0xffff0000, v53
	v_pk_fma_f32 v[52:53], v[32:33], v[32:33], v[74:75] op_sel_hi:[1,1,0]
	v_pk_add_f32 v[68:69], v[60:61], v[68:69]
	v_pk_fma_f32 v[74:75], v[58:59], v[58:59], v[86:87]
	v_lshlrev_b32_e32 v87, 16, v54
	v_and_b32_e32 v61, 0xffff0000, v54
	v_mov_b32_e32 v86, v52
	v_mov_b32_e32 v90, v80
	v_pk_add_f32 v[80:81], v[52:53], v[80:81]
	v_mul_f32_e32 v52, v49, v49
	v_mul_f32_e32 v54, v51, v51
	v_pk_add_f32 v[68:69], v[68:69], v[72:73]
	v_mov_b32_e32 v91, v87
	v_mov_b32_e32 v56, v58
	v_mov_b32_e32 v57, v42
	v_mov_b32_e32 v42, v59
	v_lshlrev_b32_e32 v58, 16, v55
	v_and_b32_e32 v59, 0xffff0000, v55
	v_pk_add_f32 v[72:73], v[74:75], v[74:75] op_sel:[0,1] op_sel_hi:[1,0]
	v_pk_fma_f32 v[74:75], v[48:49], v[48:49], v[52:53] op_sel_hi:[1,1,0]
	v_pk_fma_f32 v[92:93], v[50:51], v[50:51], v[54:55] op_sel_hi:[1,1,0]
	v_and_b32_e32 v53, 0xffff0000, v62
	v_and_b32_e32 v55, 0xffff0000, v63
	v_add_f32_e32 v96, v68, v69
	v_pk_mul_f32 v[68:69], v[86:87], v[90:91]
	v_mul_f32_e32 v81, v61, v61
	v_mul_f32_e32 v94, v58, v58
	v_mul_f32_e32 v95, v59, v59
; __device__ __forceinline__ float bf2f(unsigned v) { return __uint_as_float(v << 16); }
; __device__ __forceinline__ void phase_final(Frame& F) {
;     ...
;         for (int q = 0; q < 4; ++q) { f32x4 v[4]; float s = 0.f;
; #pragma unroll
;             for (int j = 0; j < 4; ++j) { v[j] = (f32x4){bf2f(w[q][j].x & 0xffffu), bf2f(w[q][j].x >> 16), bf2f(w[q][j].y & 0xffffu), bf2f(w[q][j].y >> 16)}; s += (v[j][0] * v[j][0] + v[j][1] * v[j][1]) + (v[j][2] * v[j][2] + v[j][3] * v[j][3]); }
;             s = wave_sum(s); const float rs = 1.0f / sqrtf(s * (1.f / DM) + EPS);
	v_lshlrev_b32_e32 v52, 16, v62
	v_lshlrev_b32_e32 v54, 16, v63
	v_mul_f32_e32 v68, v55, v55
	v_mul_f32_e32 v90, v53, v53
	v_mov_b32_e32 v73, v81
	v_mov_b32_e32 v75, v94
	v_mov_b32_e32 v93, v95
	v_and_b32_e32 v63, 0xffff0000, v65
	v_and_b32_e32 v62, 0xffff0000, v64
	v_add_f32_dpp v96, v96, v96 quad_perm:[1,0,3,2] row_mask:0xf bank_mask:0xf bound_ctrl:1
	v_mov_b32_e32 v81, v69
	v_pk_fma_f32 v[94:95], v[54:55], v[54:55], v[68:69] op_sel_hi:[1,1,0]
	v_pk_fma_f32 v[90:91], v[52:53], v[52:53], v[90:91] op_sel_hi:[1,1,0]
	v_mov_b32_e32 v60, v87
	v_lshlrev_b32_e32 v87, 16, v65
	v_lshlrev_b32_e32 v86, 16, v64
	v_pk_add_f32 v[92:93], v[74:75], v[92:93]
	v_pk_mul_f32 v[74:75], v[62:63], v[62:63]
	v_and_b32_e32 v65, 0xffff0000, v66
	v_add_f32_dpp v99, v96, v96 quad_perm:[2,3,0,1] row_mask:0xf bank_mask:0xf bound_ctrl:1
	v_pk_add_f32 v[80:81], v[80:81], v[72:73]
	v_lshlrev_b32_e32 v97, 16, v70
	v_mov_b32_e32 v96, v90
	v_pk_add_f32 v[90:91], v[90:91], v[94:95]
	v_lshlrev_b32_e32 v64, 16, v66
	v_lshlrev_b32_e32 v66, 16, v67
	v_and_b32_e32 v67, 0xffff0000, v67
	v_mov_b32_e32 v68, v86
	v_mov_b32_e32 v69, v62
	v_mov_b32_e32 v62, v87
	v_pk_fma_f32 v[86:87], v[86:87], v[86:87], v[74:75]
	v_and_b32_e32 v75, 0xffff0000, v70
	v_mov_b32_e32 v98, v94
	v_mul_f32_e32 v70, v65, v65
	v_add_f32_dpp v91, v99, v99 row_half_mirror row_mask:0xf bank_mask:0xf bound_ctrl:1
	v_pk_add_f32 v[80:81], v[80:81], v[92:93]
	v_mov_b32_e32 v99, v97
	v_lshlrev_b32_e32 v72, 16, v71
	v_and_b32_e32 v73, 0xffff0000, v71
	v_mul_f32_e32 v74, v67, v67
	v_pk_add_f32 v[92:93], v[86:87], v[86:87] op_sel:[0,1] op_sel_hi:[1,0]
	v_pk_fma_f32 v[86:87], v[64:65], v[64:65], v[70:71] op_sel_hi:[1,1,0]
	v_lshlrev_b32_e32 v70, 16, v76
	v_and_b32_e32 v71, 0xffff0000, v76
	v_lshlrev_b32_e32 v76, 16, v77
	v_and_b32_e32 v77, 0xffff0000, v77
	v_add_f32_e32 v103, v80, v81
	v_pk_mul_f32 v[80:81], v[96:97], v[98:99]
	v_mul_f32_e32 v100, v75, v75
	v_mul_f32_e32 v101, v72, v72
	v_mul_f32_e32 v102, v73, v73
	v_pk_fma_f32 v[94:95], v[66:67], v[66:67], v[74:75] op_sel_hi:[1,1,0]
	v_mov_b32_e32 v74, v97
	v_add_f32_dpp v91, v91, v91 row_mirror row_mask:0xf bank_mask:0xf bound_ctrl:1
	v_mul_f32_e32 v80, v77, v77
	v_lshlrev_b32_e32 v97, 16, v79
	v_lshlrev_b32_e32 v96, 16, v78
	v_and_b32_e32 v79, 0xffff0000, v79
	v_and_b32_e32 v78, 0xffff0000, v78
	v_mul_f32_e32 v98, v71, v71
	v_lshlrev_b32_e32 v99, 16, v84
	v_mov_b32_e32 v93, v100
	v_mov_b32_e32 v87, v101
	v_mov_b32_e32 v95, v102
	v_readlane_b32 s0, v91, 0
	v_readlane_b32 s2, v91, 16
	v_readlane_b32 s1, v91, 32
	v_readlane_b32 s3, v91, 48
	v_add_f32_dpp v110, v103, v103 quad_perm:[1,0,3,2] row_mask:0xf bank_mask:0xf bound_ctrl:1
	v_mov_b32_e32 v91, v81
	v_pk_fma_f32 v[100:101], v[76:77], v[76:77], v[80:81] op_sel_hi:[1,1,0]
	v_pk_mul_f32 v[102:103], v[78:79], v[78:79]
	v_pk_fma_f32 v[104:105], v[70:71], v[70:71], v[98:99] op_sel_hi:[1,1,0]
	v_pk_add_f32 v[94:95], v[86:87], v[94:95]
	v_lshlrev_b32_e32 v80, 16, v82
	v_and_b32_e32 v81, 0xffff0000, v82
	v_lshlrev_b32_e32 v82, 16, v83
	v_and_b32_e32 v83, 0xffff0000, v83
	v_and_b32_e32 v87, 0xffff0000, v84
	v_mov_b32_e32 v106, v96
	v_mov_b32_e32 v107, v78
	v_mov_b32_e32 v78, v97
	v_mov_b32_e32 v108, s2
	v_mov_b32_e32 v109, s3
	v_pk_add_f32 v[90:91], v[90:91], v[92:93]
	v_pk_fma_f32 v[92:93], v[96:97], v[96:97], v[102:103]
	v_mov_b32_e32 v98, v104
	v_mov_b32_e32 v96, v100
	v_mov_b32_e32 v97, v99
	v_lshlrev_b32_e32 v84, 16, v85
	v_and_b32_e32 v85, 0xffff0000, v85
	v_add_f32_dpp v110, v110, v110 quad_perm:[2,3,0,1] row_mask:0xf bank_mask:0xf bound_ctrl:1
	v_mul_f32_e32 v103, v87, v87
	v_pk_add_f32 v[100:101], v[104:105], v[100:101]
	v_mul_f32_e32 v102, v81, v81
	v_mul_f32_e32 v104, v83, v83
	v_pk_add_f32 v[108:109], s[0:1], v[108:109]
	v_pk_add_f32 v[90:91], v[90:91], v[94:95]
	v_pk_mul_f32 v[94:95], v[98:99], v[96:97]
	v_mul_f32_e32 v111, v84, v84
	v_mul_f32_e32 v112, v85, v85
	v_mov_b32_e32 v86, v99
	v_add_f32_dpp v101, v110, v110 row_half_mirror row_mask:0xf bank_mask:0xf bound_ctrl:1
	v_pk_add_f32 v[92:93], v[92:93], v[92:93] op_sel:[0,1] op_sel_hi:[1,0]
	v_pk_fma_f32 v[96:97], v[80:81], v[80:81], v[102:103] op_sel_hi:[1,1,0]
	v_pk_fma_f32 v[98:99], v[82:83], v[82:83], v[104:105] op_sel_hi:[1,1,0]
	v_add_f32_e32 v94, v108, v109
	v_add_f32_dpp v102, v101, v101 row_mirror row_mask:0xf bank_mask:0xf bound_ctrl:1
	v_add_f32_e32 v90, v90, v91
	v_mov_b32_e32 v101, v95
	v_mov_b32_e32 v93, v103
	v_mov_b32_e32 v97, v111
	v_mov_b32_e32 v99, v112
	v_fmamk_f32 v103, v94, 0x3a800000, v88
	v_readlane_b32 s0, v102, 0
	v_readlane_b32 s2, v102, 16
	v_readlane_b32 s1, v102, 32
	v_readlane_b32 s3, v102, 48
	v_add_f32_dpp v102, v90, v90 quad_perm:[1,0,3,2] row_mask:0xf bank_mask:0xf bound_ctrl:1
	v_pk_add_f32 v[90:91], v[100:101], v[92:93]
	v_pk_add_f32 v[92:93], v[96:97], v[98:99]
	v_mul_f32_e32 v96, 0x4f800000, v103
	v_cmp_gt_f32_e32 vcc, s11, v103
	v_mov_b32_e32 v94, s2
	v_mov_b32_e32 v95, s3
	v_add_f32_dpp v97, v102, v102 quad_perm:[2,3,0,1] row_mask:0xf bank_mask:0xf bound_ctrl:1
	v_pk_add_f32 v[90:91], v[90:91], v[92:93]
	v_cndmask_b32_e32 v96, v103, v96, vcc
	v_pk_add_f32 v[92:93], s[0:1], v[94:95]
	v_add_f32_dpp v94, v97, v97 row_half_mirror row_mask:0xf bank_mask:0xf bound_ctrl:1
	v_add_f32_e32 v90, v90, v91
	v_sqrt_f32_e32 v95, v96
	v_add_f32_e32 v91, v92, v93
	v_add_f32_dpp v92, v94, v94 row_mirror row_mask:0xf bank_mask:0xf bound_ctrl:1
	v_add_f32_dpp v90, v90, v90 quad_perm:[1,0,3,2] row_mask:0xf bank_mask:0xf bound_ctrl:1
	v_fmamk_f32 v93, v91, 0x3a800000, v88
	v_readlane_b32 s2, v92, 0
	v_readlane_b32 s0, v92, 16
	v_readlane_b32 s3, v92, 32
	v_readlane_b32 s1, v92, 48
	v_add_f32_dpp v92, v90, v90 quad_perm:[2,3,0,1] row_mask:0xf bank_mask:0xf bound_ctrl:1
; __device__ __forceinline__ void phase_final(Frame& F) {
;     ...
;             s = wave_sum(s); const float rs = 1.0f / sqrtf(s * (1.f / DM) + EPS);
;             f32x4* o = (f32x4*)(P.out + (size_t)(row0 + q) * DM) + F.lane;
; #pragma unroll
;             for (int j = 0; j < 4; ++j) o[64 * j] = v[j] * rs * gv[j]; }
	v_mul_f32_e32 v94, 0x4f800000, v93
	v_mov_b32_e32 v90, s0
	v_mov_b32_e32 v91, s1
	v_add_f32_dpp v92, v92, v92 row_half_mirror row_mask:0xf bank_mask:0xf bound_ctrl:1
	v_cmp_gt_f32_e64 s[0:1], s11, v93
	v_pk_add_f32 v[90:91], s[2:3], v[90:91]
	v_add_f32_dpp v92, v92, v92 row_mirror row_mask:0xf bank_mask:0xf bound_ctrl:1
	v_cndmask_b32_e64 v93, v93, v94, s[0:1]
	v_add_u32_e32 v94, -1, v95
	v_add_u32_e32 v97, 1, v95
	v_sqrt_f32_e32 v98, v93
	v_add_f32_e32 v90, v90, v91
	v_readlane_b32 s4, v92, 0
	v_readlane_b32 s2, v92, 16
	v_readlane_b32 s5, v92, 32
	v_readlane_b32 s3, v92, 48
	v_fma_f32 v92, -v94, v95, v96
	v_fma_f32 v99, -v97, v95, v96
	v_fmamk_f32 v100, v90, 0x3a800000, v88
	v_mov_b32_e32 v90, s2
	v_mov_b32_e32 v91, s3
	v_cmp_ge_f32_e64 s[2:3], 0, v92
	v_pk_add_f32 v[90:91], s[4:5], v[90:91]
	v_cmp_lt_f32_e64 s[4:5], 0, v99
	v_cndmask_b32_e64 v92, v95, v94, s[2:3]
	v_mul_f32_e32 v94, 0x4f800000, v100
	v_cmp_gt_f32_e64 s[2:3], s11, v100
	v_cndmask_b32_e64 v92, v92, v97, s[4:5]
	v_add_f32_e32 v90, v90, v91
	v_cndmask_b32_e64 v94, v100, v94, s[2:3]
	v_mul_f32_e32 v91, 0x37800000, v92
	v_add_u32_e32 v95, -1, v98
	v_add_u32_e32 v97, 1, v98
	v_sqrt_f32_e32 v99, v94
	v_cndmask_b32_e32 v91, v92, v91, vcc
	v_fma_f32 v92, -v95, v98, v93
	v_cmp_class_f32_e64 s[4:5], v96, v89
	v_fmamk_f32 v90, v90, 0x3a800000, v88
	v_fma_f32 v100, -v97, v98, v93
	v_cndmask_b32_e64 v91, v91, v96, s[4:5]
	v_cmp_ge_f32_e64 s[4:5], 0, v92
	v_mul_f32_e32 v101, 0x4f800000, v90
	v_cmp_gt_f32_e32 vcc, s11, v90
	v_cndmask_b32_e64 v92, v98, v95, s[4:5]
	v_cmp_lt_f32_e64 s[4:5], 0, v100
	v_cndmask_b32_e32 v90, v90, v101, vcc
	v_add_u32_e32 v101, -1, v99
	v_cndmask_b32_e64 v92, v92, v97, s[4:5]
	v_sqrt_f32_e32 v97, v90
	v_mul_f32_e32 v100, 0x37800000, v92
	v_div_scale_f32 v95, s[6:7], v91, v91, 1.0
	v_add_u32_e32 v102, 1, v99
	v_cndmask_b32_e64 v92, v92, v100, s[0:1]
	v_fma_f32 v100, -v101, v99, v94
	v_cmp_class_f32_e64 s[0:1], v93, v89
	v_rcp_f32_e32 v98, v95
	v_fma_f32 v103, -v102, v99, v94
	v_cndmask_b32_e64 v104, v92, v93, s[0:1]
	v_cmp_ge_f32_e64 s[0:1], 0, v100
	v_add_u32_e32 v93, -1, v97
	v_fma_f32 v108, -v93, v97, v90
	v_cndmask_b32_e64 v92, v99, v101, s[0:1]
	v_cmp_lt_f32_e64 s[0:1], 0, v103
	v_div_scale_f32 v99, s[4:5], v104, v104, 1.0
	s_nop 0
	v_cndmask_b32_e64 v92, v92, v102, s[0:1]
	v_add_u32_e32 v101, 1, v97
	v_mul_f32_e32 v105, 0x37800000, v92
	v_fma_f32 v102, -v95, v98, 1.0
	v_rcp_f32_e32 v103, v99
	v_fma_f32 v109, -v101, v97, v90
	v_cndmask_b32_e64 v92, v92, v105, s[2:3]
	v_cmp_ge_f32_e64 s[2:3], 0, v108
	v_div_scale_f32 v96, s[6:7], 1.0, v91, 1.0
	v_fmac_f32_e32 v98, v102, v98
	v_cmp_class_f32_e64 s[0:1], v94, v89
	v_cndmask_b32_e64 v93, v97, v93, s[2:3]
	v_cmp_lt_f32_e64 s[2:3], 0, v109
	v_mul_f32_e32 v97, v96, v98
	v_cndmask_b32_e64 v102, v92, v94, s[0:1]
	v_cndmask_b32_e64 v92, v93, v101, s[2:3]
	v_fma_f32 v93, -v95, v97, v96
	v_div_scale_f32 v101, s[0:1], v102, v102, 1.0
	v_mul_f32_e32 v94, 0x37800000, v92
	v_fmac_f32_e32 v97, v93, v98
	v_fma_f32 v93, -v99, v103, 1.0
	v_rcp_f32_e32 v108, v101
	v_cndmask_b32_e32 v92, v92, v94, vcc
	v_cmp_class_f32_e32 vcc, v90, v89
	v_div_scale_f32 v100, s[4:5], 1.0, v104, 1.0
	v_fma_f32 v94, -v95, v97, v96
	v_fmac_f32_e32 v103, v93, v103
	v_cndmask_b32_e32 v109, v92, v90, vcc
	s_mov_b64 vcc, s[6:7]
	v_div_fmas_f32 v90, v94, v98, v97
	v_mul_f32_e32 v98, v100, v103
	v_div_scale_f32 v110, s[2:3], v109, v109, 1.0
	v_div_fixup_f32 v90, v90, v91, 1.0
	v_fma_f32 v112, -v99, v98, v100
	v_rcp_f32_e32 v113, v110
	v_pk_mul_f32 v[24:25], v[90:91], v[24:25] op_sel_hi:[0,1]
	v_pk_mul_f32 v[28:29], v[90:91], v[28:29] op_sel_hi:[0,1]
	v_pk_mul_f32 v[34:35], v[90:91], v[34:35] op_sel_hi:[0,1]
	v_fmac_f32_e32 v98, v112, v103
	v_fma_f32 v112, -v101, v108, 1.0
	v_div_scale_f32 v105, s[0:1], 1.0, v102, 1.0
	v_pk_mul_f32 v[92:93], v[90:91], v[40:41] op_sel_hi:[0,1]
	v_pk_mul_f32 v[40:41], v[90:91], v[30:31] op_sel_hi:[0,1]
	v_pk_mul_f32 v[94:95], v[90:91], v[38:39] op_sel_hi:[0,1]
	v_pk_mul_f32 v[96:97], v[46:47], v[90:91] op_sel_hi:[1,0]
	v_pk_mul_f32 v[90:91], v[44:45], v[90:91] op_sel_hi:[1,0]
	v_pk_mul_f32 v[30:31], v[2:3], v[28:29]
	v_pk_mul_f32 v[28:29], v[0:1], v[24:25]
	v_pk_mul_f32 v[44:45], v[8:9], v[34:35]
	v_fma_f32 v24, -v99, v98, v100
	v_fmac_f32_e32 v108, v112, v108
	s_mov_b64 vcc, s[4:5]
; __device__ __forceinline__ void phase_final(Frame& F) {
;     ...
;             f32x4* o = (f32x4*)(P.out + (size_t)(row0 + q) * DM) + F.lane;
; #pragma unroll
;             for (int j = 0; j < 4; ++j) o[64 * j] = v[j] * rs * gv[j]; }
	v_pk_mul_f32 v[40:41], v[6:7], v[40:41]
	v_pk_mul_f32 v[38:39], v[4:5], v[92:93]
	v_pk_mul_f32 v[46:47], v[10:11], v[94:95]
	v_pk_mul_f32 v[92:93], v[14:15], v[90:91]
	v_pk_mul_f32 v[90:91], v[12:13], v[96:97]
	global_store_dwordx4 v[20:21], v[28:31], off offset:-3072 nt
	global_store_dwordx4 v[20:21], v[38:41], off offset:-2048 nt
	global_store_dwordx4 v[20:21], v[44:47], off offset:-1024 nt
	global_store_dwordx4 v[22:23], v[90:93], off offset:-4096 nt
	v_div_fmas_f32 v20, v24, v103, v98
	v_mul_f32_e32 v44, v105, v108
	v_div_fixup_f32 v20, v20, v104, 1.0
	v_fma_f32 v30, -v101, v44, v105
	v_fma_f32 v31, -v110, v113, 1.0
	v_div_scale_f32 v111, s[2:3], 1.0, v109, 1.0
	v_pk_mul_f32 v[24:25], v[20:21], v[32:33] op_sel_hi:[0,1]
	v_pk_mul_f32 v[28:29], v[20:21], v[36:37] op_sel_hi:[0,1]
	v_pk_mul_f32 v[32:33], v[20:21], v[56:57] op_sel_hi:[0,1]
	v_pk_mul_f32 v[34:35], v[20:21], v[42:43] op_sel_hi:[0,1]
	v_pk_mul_f32 v[36:37], v[20:21], v[48:49] op_sel_hi:[0,1]
	v_pk_mul_f32 v[38:39], v[20:21], v[50:51] op_sel_hi:[0,1]
	v_pk_mul_f32 v[40:41], v[60:61], v[20:21] op_sel_hi:[1,0]
	v_pk_mul_f32 v[20:21], v[58:59], v[20:21] op_sel_hi:[1,0]
	v_fmac_f32_e32 v44, v30, v108
	v_fmac_f32_e32 v113, v31, v113
	v_pk_mul_f32 v[42:43], v[14:15], v[20:21]
	v_fma_f32 v20, -v101, v44, v105
	v_mul_f32_e32 v45, v111, v113
	s_mov_b64 vcc, s[0:1]
	v_div_fmas_f32 v20, v20, v108, v44
	v_fma_f32 v21, -v110, v45, v111
	v_pk_mul_f32 v[30:31], v[2:3], v[28:29]
	v_pk_mul_f32 v[28:29], v[0:1], v[24:25]
	v_pk_mul_f32 v[40:41], v[12:13], v[40:41]
	v_div_fixup_f32 v20, v20, v102, 1.0
	v_fmac_f32_e32 v45, v21, v113
	v_pk_mul_f32 v[34:35], v[6:7], v[34:35]
	v_pk_mul_f32 v[32:33], v[4:5], v[32:33]
	v_pk_mul_f32 v[38:39], v[10:11], v[38:39]
	v_pk_mul_f32 v[36:37], v[8:9], v[36:37]
	global_store_dwordx4 v[22:23], v[28:31], off offset:-3072 nt
	global_store_dwordx4 v[22:23], v[32:35], off offset:-2048 nt
	global_store_dwordx4 v[22:23], v[36:39], off offset:-1024 nt
	global_store_dwordx4 v[22:23], v[40:43], off nt
	v_pk_mul_f32 v[24:25], v[20:21], v[52:53] op_sel_hi:[0,1]
	v_pk_mul_f32 v[22:23], v[20:21], v[54:55] op_sel_hi:[0,1]
	v_fma_f32 v40, -v110, v45, v111
	s_mov_b64 vcc, s[2:3]
	v_pk_mul_f32 v[28:29], v[20:21], v[68:69] op_sel_hi:[0,1]
	v_pk_mul_f32 v[30:31], v[20:21], v[62:63] op_sel_hi:[0,1]
	v_pk_mul_f32 v[32:33], v[20:21], v[64:65] op_sel_hi:[0,1]
	v_pk_mul_f32 v[34:35], v[20:21], v[66:67] op_sel_hi:[0,1]
	v_pk_mul_f32 v[36:37], v[74:75], v[20:21] op_sel_hi:[1,0]
	v_pk_mul_f32 v[38:39], v[72:73], v[20:21] op_sel_hi:[1,0]
	v_pk_mul_f32 v[22:23], v[2:3], v[22:23]
	v_pk_mul_f32 v[20:21], v[0:1], v[24:25]
	v_div_fmas_f32 v24, v40, v113, v45
	v_pk_mul_f32 v[30:31], v[6:7], v[30:31]
	v_pk_mul_f32 v[28:29], v[4:5], v[28:29]
	v_pk_mul_f32 v[34:35], v[10:11], v[34:35]
	v_pk_mul_f32 v[32:33], v[8:9], v[32:33]
	v_pk_mul_f32 v[38:39], v[14:15], v[38:39]
	v_pk_mul_f32 v[36:37], v[12:13], v[36:37]
	global_store_dwordx4 v[26:27], v[20:23], off offset:-3072 nt
	global_store_dwordx4 v[26:27], v[28:31], off offset:-2048 nt
	global_store_dwordx4 v[26:27], v[32:35], off offset:-1024 nt
	global_store_dwordx4 v[16:17], v[36:39], off offset:-4096 nt
	v_div_fixup_f32 v20, v24, v109, 1.0
	v_pk_mul_f32 v[24:25], v[20:21], v[70:71] op_sel_hi:[0,1]
	v_pk_mul_f32 v[22:23], v[20:21], v[76:77] op_sel_hi:[0,1]
	v_pk_mul_f32 v[28:29], v[20:21], v[106:107] op_sel_hi:[0,1]
	v_pk_mul_f32 v[26:27], v[20:21], v[78:79] op_sel_hi:[0,1]
	v_pk_mul_f32 v[32:33], v[20:21], v[80:81] op_sel_hi:[0,1]
	v_pk_mul_f32 v[30:31], v[20:21], v[82:83] op_sel_hi:[0,1]
	v_pk_mul_f32 v[36:37], v[86:87], v[20:21] op_sel_hi:[1,0]
	v_pk_mul_f32 v[34:35], v[84:85], v[20:21] op_sel_hi:[1,0]
	v_pk_mul_f32 v[22:23], v[2:3], v[22:23]
	v_pk_mul_f32 v[20:21], v[0:1], v[24:25]
	v_pk_mul_f32 v[26:27], v[6:7], v[26:27]
	v_pk_mul_f32 v[24:25], v[4:5], v[28:29]
	v_pk_mul_f32 v[30:31], v[10:11], v[30:31]
	v_pk_mul_f32 v[28:29], v[8:9], v[32:33]
	v_pk_mul_f32 v[34:35], v[14:15], v[34:35]
	v_pk_mul_f32 v[32:33], v[12:13], v[36:37]
	global_store_dwordx4 v[16:17], v[20:23], off offset:-3072 nt
	global_store_dwordx4 v[16:17], v[24:27], off offset:-2048 nt
	global_store_dwordx4 v[16:17], v[28:31], off offset:-1024 nt
	global_store_dwordx4 v[16:17], v[32:35], off nt
	v_lshl_add_u64 v[16:17], v[16:17], 0, s[12:13]
	s_cbranch_scc1 .LBB0_1563
